# phase 9 epilogue: the dead sub-list position search (five dependent LDS reads per row block) removed now that the token entry comes from the prologue prefetch
# speedup vs baseline: 1.0029x; 1.0029x over previous
.LBB0_1093:
	s_waitcnt vmcnt(0)
	s_lshl_b32 s10, s34, 13
	s_mulk_i32 s34, 0x44
	s_add_i32 s36, s34, 0
	s_add_i32 s36, s36, 0x20400
	v_cmp_gt_i32_e32 vcc, s48, v164
	s_and_saveexec_b64 s[34:35], vcc
	s_cbranch_execz .LBB0_1095
	v_mov_b32_e32 v130, s36

	v_add_u32_e32 v131, s47, v164
	v_med3_f32 v134, v51, s45, v168
	v_med3_f32 v135, v53, s45, v168
	v_add_u32_e32 v53, s10, v131
	s_waitcnt lgkmcnt(0)
	v_cmp_gt_i32_e32 vcc, v130, v131
	v_med3_f32 v139, v18, s45, v168
	v_med3_f32 v140, v19, s45, v168
	v_cndmask_b32_e64 v130, 8, 0, vcc
	v_lshl_add_u32 v132, v130, 2, s36

	v_or_b32_e32 v133, 4, v130
	v_mov_b32_e32 v18, v147
	v_cvt_pk_fp8_f32 v18, v139, v140
	v_med3_f32 v20, v20, s45, v168
	s_waitcnt lgkmcnt(0)
	v_cmp_gt_i32_e32 vcc, v132, v131
	v_med3_f32 v21, v21, s45, v168
	v_cvt_pk_fp8_f32 v18, v20, v21 op_sel:[0,0,1]
	v_cndmask_b32_e32 v130, v133, v130, vcc
	v_lshl_add_u32 v132, v130, 2, s36

	v_med3_f32 v133, v50, s45, v168
	v_or_b32_e32 v50, 2, v130
	v_med3_f32 v22, v22, s45, v168
	v_med3_f32 v23, v23, s45, v168
	s_waitcnt lgkmcnt(0)
	v_cmp_gt_i32_e32 vcc, v132, v131
	v_med3_f32 v132, v52, s45, v168
	v_mov_b32_e32 v19, v147
	v_cndmask_b32_e32 v51, v50, v130, vcc
	v_lshl_add_u32 v50, v51, 2, s36

	v_or_b32_e32 v52, 1, v51
	v_cvt_pk_fp8_f32 v19, v22, v23
	v_med3_f32 v26, v26, s45, v168
	v_mov_b32_e32 v50, v147
	s_waitcnt lgkmcnt(0)
	v_cmp_gt_i32_e32 vcc, v130, v131
	v_med3_f32 v54, v54, s45, v168
	v_med3_f32 v55, v55, s45, v168
	v_cndmask_b32_e32 v51, v52, v51, vcc
	v_lshl_add_u32 v52, v51, 2, s36

	v_med3_f32 v58, v58, s45, v168
	v_med3_f32 v59, v59, s45, v168
	v_med3_f32 v62, v62, s45, v168
	v_med3_f32 v63, v63, s45, v168
	s_waitcnt lgkmcnt(0)
	v_sub_u32_e32 v52, v53, v52
	v_lshl_add_u32 v52, v51, 9, v52
	v_ashrrev_i32_e32 v53, 31, v52
	v_lshl_add_u64 v[52:53], v[52:53], 2, s[8:9]
	v_mov_b32_e32 v130, v210
	v_mov_b32_e32 v51, v147
	v_mov_b32_e32 v52, v147
	v_mov_b32_e32 v53, v147
	v_med3_f32 v131, v34, s45, v168
	v_med3_f32 v136, v35, s45, v168
	v_med3_f32 v137, v36, s45, v168
	v_med3_f32 v138, v37, s45, v168
	v_mov_b32_e32 v34, v147
	v_med3_f32 v38, v38, s45, v168
	v_med3_f32 v39, v39, s45, v168
	v_mov_b32_e32 v35, v147
	v_med3_f32 v42, v42, s45, v168
	v_med3_f32 v43, v43, s45, v168
	v_mov_b32_e32 v36, v147
	v_med3_f32 v46, v46, s45, v168
	v_med3_f32 v47, v47, s45, v168
	v_mov_b32_e32 v37, v147
	v_cvt_pk_fp8_f32 v50, v133, v134
	v_cvt_pk_fp8_f32 v51, v54, v55
	v_cvt_pk_fp8_f32 v52, v58, v59
	v_cvt_pk_fp8_f32 v53, v62, v63
	v_med3_f32 v24, v24, s45, v168
	v_med3_f32 v25, v25, s45, v168
	v_cvt_pk_fp8_f32 v34, v131, v136
	v_cvt_pk_fp8_f32 v35, v38, v39
	v_cvt_pk_fp8_f32 v36, v42, v43
	v_cvt_pk_fp8_f32 v37, v46, v47
	v_cvt_pk_fp8_f32 v19, v24, v25 op_sel:[0,0,1]
	v_med3_f32 v24, v28, s45, v168
	v_med3_f32 v25, v29, s45, v168
	v_med3_f32 v56, v56, s45, v168
	v_med3_f32 v57, v57, s45, v168
	v_med3_f32 v60, v60, s45, v168
	v_med3_f32 v61, v61, s45, v168
	v_med3_f32 v64, v64, s45, v168
	v_med3_f32 v65, v65, s45, v168
	v_med3_f32 v40, v40, s45, v168
	v_med3_f32 v41, v41, s45, v168
	v_med3_f32 v44, v44, s45, v168
	v_med3_f32 v45, v45, s45, v168
	v_med3_f32 v48, v48, s45, v168
	v_med3_f32 v49, v49, s45, v168
	v_cvt_pk_fp8_f32 v50, v132, v135 op_sel:[0,0,1]
	v_cvt_pk_fp8_f32 v51, v56, v57 op_sel:[0,0,1]
	v_cvt_pk_fp8_f32 v52, v60, v61 op_sel:[0,0,1]
	v_cvt_pk_fp8_f32 v53, v64, v65 op_sel:[0,0,1]
	v_cvt_pk_fp8_f32 v34, v137, v138 op_sel:[0,0,1]
	v_cvt_pk_fp8_f32 v35, v40, v41 op_sel:[0,0,1]
	v_cvt_pk_fp8_f32 v36, v44, v45 op_sel:[0,0,1]
	v_cvt_pk_fp8_f32 v37, v48, v49 op_sel:[0,0,1]
	v_permlane32_swap_b32_e32 v50, v51
	v_permlane32_swap_b32_e32 v52, v53
	v_permlane32_swap_b32_e32 v18, v19
	v_permlane32_swap_b32_e32 v34, v35
	v_permlane32_swap_b32_e32 v36, v37
	v_permlane32_swap_b32_e32 v50, v52
	v_permlane32_swap_b32_e32 v51, v53
	v_permlane32_swap_b32_e32 v34, v36
	v_permlane32_swap_b32_e32 v35, v37
	v_med3_f32 v3, v3, s45, v168
	v_med3_f32 v6, v6, s45, v168
	v_med3_f32 v7, v7, s45, v168
	v_med3_f32 v4, v4, s45, v168
	v_med3_f32 v5, v5, s45, v168
	s_waitcnt vmcnt(0)
	v_ashrrev_i32_e32 v20, 16, v130
	v_ashrrev_i32_e32 v21, 31, v20
	v_lshlrev_b32_e32 v22, 11, v130
	v_lshlrev_b64 v[20:21], 24, v[20:21]
	v_and_b32_e32 v146, 0x7fff800, v22
	v_lshl_add_u64 v[20:21], s[18:19], 0, v[20:21]
	v_lshl_add_u64 v[20:21], v[20:21], 0, v[146:147]
	v_lshl_add_u64 v[20:21], v[20:21], 0, s[30:31]
	v_lshl_add_u64 v[22:23], v[20:21], 0, v[150:151]
	v_med3_f32 v21, v27, s45, v168
	v_mov_b32_e32 v20, v147
	v_cvt_pk_fp8_f32 v20, v26, v21
	v_med3_f32 v26, v30, s45, v168
	v_med3_f32 v27, v31, s45, v168
	v_mov_b32_e32 v21, v147
	v_cvt_pk_fp8_f32 v21, v26, v27
	v_cvt_pk_fp8_f32 v20, v24, v25 op_sel:[0,0,1]
	v_med3_f32 v24, v32, s45, v168
	v_med3_f32 v25, v33, s45, v168
	v_cvt_pk_fp8_f32 v21, v24, v25 op_sel:[0,0,1]
	global_store_dwordx4 v[22:23], v[50:53], off
	global_store_dwordx4 v[22:23], v[34:37], off offset:32
	v_permlane32_swap_b32_e32 v20, v21
	s_nop 1
	v_permlane32_swap_b32_e32 v18, v20
	v_permlane32_swap_b32_e32 v19, v21
	global_store_dwordx4 v[22:23], v[18:21], off offset:64
	s_nop 1
	v_med3_f32 v18, v2, s45, v168
	v_mov_b32_e32 v2, v147
	v_cvt_pk_fp8_f32 v2, v18, v3
	v_mov_b32_e32 v3, v147
	v_cvt_pk_fp8_f32 v3, v6, v7
	v_med3_f32 v6, v11, s45, v168
	v_cvt_pk_fp8_f32 v2, v4, v5 op_sel:[0,0,1]
	v_med3_f32 v4, v8, s45, v168
	v_med3_f32 v5, v9, s45, v168
	v_cvt_pk_fp8_f32 v3, v4, v5 op_sel:[0,0,1]
	v_med3_f32 v5, v10, s45, v168
	v_mov_b32_e32 v4, v147
	v_cvt_pk_fp8_f32 v4, v5, v6
	v_med3_f32 v6, v14, s45, v168
	v_med3_f32 v9, v15, s45, v168
	v_mov_b32_e32 v5, v147
	v_cvt_pk_fp8_f32 v5, v6, v9
	v_med3_f32 v7, v12, s45, v168
	v_med3_f32 v8, v13, s45, v168
	v_cvt_pk_fp8_f32 v4, v7, v8 op_sel:[0,0,1]
	v_med3_f32 v6, v16, s45, v168
	v_med3_f32 v7, v17, s45, v168
	v_cvt_pk_fp8_f32 v5, v6, v7 op_sel:[0,0,1]
	v_permlane32_swap_b32_e32 v2, v3
	s_nop 0
	v_permlane32_swap_b32_e32 v4, v5
	s_nop 1
	v_permlane32_swap_b32_e32 v2, v4
	v_permlane32_swap_b32_e32 v3, v5
	global_store_dwordx4 v[22:23], v[2:5], off offset:96
.LBB0_1095:
	s_or_b64 exec, exec, s[34:35]
	v_cmp_gt_i32_e32 vcc, s48, v166
	s_and_saveexec_b64 s[34:35], vcc
	s_cbranch_execz .LBB0_1082
	v_mov_b32_e32 v2, s36

	v_add_u32_e32 v3, s47, v166
	v_med3_f32 v12, v114, s45, v168
	v_med3_f32 v13, v115, s45, v168
	v_med3_f32 v16, v118, s45, v168
	s_waitcnt lgkmcnt(0)
	v_cmp_gt_i32_e32 vcc, v2, v3
	v_med3_f32 v17, v119, s45, v168
	v_med3_f32 v21, v122, s45, v168
	v_cndmask_b32_e64 v2, 8, 0, vcc
	v_lshl_add_u32 v4, v2, 2, s36

	v_or_b32_e32 v5, 4, v2
	v_med3_f32 v22, v123, s45, v168
	v_med3_f32 v25, v126, s45, v168
	v_med3_f32 v26, v127, s45, v168
	s_waitcnt lgkmcnt(0)
	v_cmp_gt_i32_e32 vcc, v4, v3
	v_med3_f32 v29, v98, s45, v168
	v_med3_f32 v30, v99, s45, v168
	v_cndmask_b32_e32 v2, v5, v2, vcc
	v_lshl_add_u32 v4, v2, 2, s36

	v_or_b32_e32 v5, 2, v2
	v_med3_f32 v33, v102, s45, v168
	v_med3_f32 v34, v103, s45, v168
	v_mov_b32_e32 v7, v147
	s_waitcnt lgkmcnt(0)
	v_cmp_gt_i32_e32 vcc, v4, v3
	v_med3_f32 v37, v106, s45, v168
	v_med3_f32 v38, v107, s45, v168
	v_cndmask_b32_e32 v4, v5, v2, vcc
	v_lshl_add_u32 v2, v4, 2, s36

	v_or_b32_e32 v6, 1, v4
	v_mov_b32_e32 v2, v147
	v_mov_b32_e32 v8, v147
	v_med3_f32 v41, v110, s45, v168
	s_waitcnt lgkmcnt(0)
	v_cmp_gt_i32_e32 vcc, v5, v3
	v_add_u32_e32 v3, s10, v3
	v_med3_f32 v42, v111, s45, v168
	v_cndmask_b32_e32 v4, v6, v4, vcc
	v_lshl_add_u32 v5, v4, 2, s36

	v_mov_b32_e32 v6, v147
	v_mov_b32_e32 v9, v147
	v_cvt_pk_fp8_f32 v2, v12, v13
	v_cvt_pk_fp8_f32 v6, v29, v30
	s_waitcnt lgkmcnt(0)
	v_sub_u32_e32 v3, v3, v5
	v_lshl_add_u32 v4, v4, 9, v3
	v_ashrrev_i32_e32 v5, 31, v4
	v_lshl_add_u64 v[4:5], v[4:5], 2, s[8:9]
	v_mov_b32_e32 v19, v211
	v_mov_b32_e32 v3, v147
	v_mov_b32_e32 v4, v147
	v_mov_b32_e32 v5, v147
	v_cvt_pk_fp8_f32 v3, v16, v17
	v_cvt_pk_fp8_f32 v4, v21, v22
	v_cvt_pk_fp8_f32 v5, v25, v26
	v_cvt_pk_fp8_f32 v7, v33, v34
	v_cvt_pk_fp8_f32 v8, v37, v38
	v_cvt_pk_fp8_f32 v9, v41, v42
	v_med3_f32 v14, v116, s45, v168
	v_med3_f32 v15, v117, s45, v168
	v_med3_f32 v18, v120, s45, v168
	v_med3_f32 v20, v121, s45, v168
	v_med3_f32 v23, v124, s45, v168
	v_med3_f32 v24, v125, s45, v168
	v_med3_f32 v27, v128, s45, v168
	v_med3_f32 v28, v129, s45, v168
	v_med3_f32 v31, v100, s45, v168
	v_med3_f32 v32, v101, s45, v168
	v_med3_f32 v35, v104, s45, v168
	v_med3_f32 v36, v105, s45, v168
	v_med3_f32 v39, v108, s45, v168
	v_med3_f32 v40, v109, s45, v168
	v_med3_f32 v43, v112, s45, v168
	v_med3_f32 v44, v113, s45, v168
	v_cvt_pk_fp8_f32 v2, v14, v15 op_sel:[0,0,1]
	v_cvt_pk_fp8_f32 v3, v18, v20 op_sel:[0,0,1]
	v_cvt_pk_fp8_f32 v4, v23, v24 op_sel:[0,0,1]
	v_cvt_pk_fp8_f32 v5, v27, v28 op_sel:[0,0,1]
	v_cvt_pk_fp8_f32 v6, v31, v32 op_sel:[0,0,1]
	v_cvt_pk_fp8_f32 v7, v35, v36 op_sel:[0,0,1]
	v_cvt_pk_fp8_f32 v8, v39, v40 op_sel:[0,0,1]
	v_cvt_pk_fp8_f32 v9, v43, v44 op_sel:[0,0,1]
	v_permlane32_swap_b32_e32 v2, v3
	v_permlane32_swap_b32_e32 v4, v5
	v_permlane32_swap_b32_e32 v6, v7
	v_permlane32_swap_b32_e32 v8, v9
	v_permlane32_swap_b32_e32 v2, v4
	v_permlane32_swap_b32_e32 v3, v5
	v_med3_f32 v53, v90, s45, v168
	v_permlane32_swap_b32_e32 v6, v8
	v_permlane32_swap_b32_e32 v7, v9
	v_med3_f32 v45, v82, s45, v168
	v_med3_f32 v46, v83, s45, v168
	v_mov_b32_e32 v10, v147
	v_med3_f32 v49, v86, s45, v168
	v_med3_f32 v50, v87, s45, v168
	v_mov_b32_e32 v11, v147
	v_cvt_pk_fp8_f32 v10, v45, v46
	v_cvt_pk_fp8_f32 v11, v49, v50
	v_med3_f32 v47, v84, s45, v168
	v_med3_f32 v48, v85, s45, v168
	v_med3_f32 v51, v88, s45, v168
	v_med3_f32 v52, v89, s45, v168
	v_cvt_pk_fp8_f32 v10, v47, v48 op_sel:[0,0,1]
	v_cvt_pk_fp8_f32 v11, v51, v52 op_sel:[0,0,1]
	s_waitcnt vmcnt(0)
	v_ashrrev_i32_e32 v12, 16, v19
	v_ashrrev_i32_e32 v13, 31, v12
	v_lshlrev_b32_e32 v14, 11, v19
	v_lshlrev_b64 v[12:13], 24, v[12:13]
	v_and_b32_e32 v146, 0x7fff800, v14
	v_lshl_add_u64 v[12:13], s[18:19], 0, v[12:13]
	v_lshl_add_u64 v[12:13], v[12:13], 0, v[146:147]
	v_lshl_add_u64 v[12:13], v[12:13], 0, s[30:31]
	v_lshl_add_u64 v[14:15], v[12:13], 0, v[150:151]
	global_store_dwordx4 v[14:15], v[2:5], off
	global_store_dwordx4 v[14:15], v[6:9], off offset:32
	v_mov_b32_e32 v12, v147
	v_med3_f32 v2, v91, s45, v168
	v_cvt_pk_fp8_f32 v12, v53, v2
	v_med3_f32 v2, v94, s45, v168
	v_med3_f32 v5, v95, s45, v168
	v_mov_b32_e32 v13, v147
	v_cvt_pk_fp8_f32 v13, v2, v5
	v_med3_f32 v3, v92, s45, v168
	v_med3_f32 v4, v93, s45, v168
	v_cvt_pk_fp8_f32 v12, v3, v4 op_sel:[0,0,1]
	v_med3_f32 v2, v96, s45, v168
	v_med3_f32 v3, v97, s45, v168
	v_cvt_pk_fp8_f32 v13, v2, v3 op_sel:[0,0,1]
	v_med3_f32 v3, v66, s45, v168
	v_med3_f32 v4, v67, s45, v168
	v_mov_b32_e32 v2, v147
	v_cvt_pk_fp8_f32 v2, v3, v4
	v_med3_f32 v4, v70, s45, v168
	v_med3_f32 v7, v71, s45, v168
	v_mov_b32_e32 v3, v147
	v_cvt_pk_fp8_f32 v3, v4, v7
	v_med3_f32 v5, v68, s45, v168
	v_med3_f32 v6, v69, s45, v168
	v_cvt_pk_fp8_f32 v2, v5, v6 op_sel:[0,0,1]
	v_med3_f32 v4, v72, s45, v168
	v_med3_f32 v5, v73, s45, v168
	v_cvt_pk_fp8_f32 v3, v4, v5 op_sel:[0,0,1]
	v_med3_f32 v5, v74, s45, v168
	v_med3_f32 v6, v75, s45, v168
	v_mov_b32_e32 v4, v147
	v_cvt_pk_fp8_f32 v4, v5, v6
	v_med3_f32 v6, v78, s45, v168
	v_med3_f32 v9, v79, s45, v168
	v_mov_b32_e32 v5, v147
	v_cvt_pk_fp8_f32 v5, v6, v9
	v_med3_f32 v7, v76, s45, v168
	v_med3_f32 v8, v77, s45, v168
	v_cvt_pk_fp8_f32 v4, v7, v8 op_sel:[0,0,1]
	v_med3_f32 v6, v80, s45, v168
	v_med3_f32 v7, v81, s45, v168
	v_cvt_pk_fp8_f32 v5, v6, v7 op_sel:[0,0,1]
	v_permlane32_swap_b32_e32 v10, v11
	v_permlane32_swap_b32_e32 v12, v13
	v_permlane32_swap_b32_e32 v2, v3
	v_permlane32_swap_b32_e32 v4, v5
	v_permlane32_swap_b32_e32 v10, v12
	v_permlane32_swap_b32_e32 v11, v13
	v_permlane32_swap_b32_e32 v2, v4
	v_permlane32_swap_b32_e32 v3, v5
	global_store_dwordx4 v[14:15], v[10:13], off offset:64
	global_store_dwordx4 v[14:15], v[2:5], off offset:96
	s_branch .LBB0_1082
